# P0 RMSNorm rows: weight-vector chunks loaded once before the loop (no per-chunk load + full drain behind the stores), on top of the P5 logits-loop rewrite
# speedup vs baseline: 1.0103x; 1.0045x over previous
.LBB0_14:
	s_lshr_b32 s94, s93, 6
	s_cmp_gt_i32 s72, 0
	v_writelane_b32 v253, s0, 21
	s_cselect_b64 s[0:1], -1, 0
	s_cmp_lt_i32 s73, 1
	s_cselect_b64 s[2:3], -1, 0
	s_or_b64 s[0:1], s[0:1], s[2:3]
	v_and_b32_e32 v198, 63, v0
	s_and_b64 vcc, exec, s[0:1]
	s_mul_i32 s47, s94, 0x4100
	s_mov_b64 s[48:49], s[72:73]
	s_cbranch_vccnz .LBB0_201
	s_lshl_b32 s0, s97, 3
	s_add_i32 s0, s0, s94
	s_lshl_b32 s2, s96, 3
	s_cmpk_gt_i32 s0, 0x1fff
	s_cbranch_scc1 .LBB0_18
	v_readlane_b32 s8, v253, 2
	v_lshlrev_b32_e32 v2, 4, v198
	v_mov_b32_e32 v3, 0
	v_readlane_b32 s10, v253, 4
	v_readlane_b32 s11, v253, 5
	s_mov_b64 s[6:7], 0x1400
	s_ashr_i32 s1, s0, 31
	v_lshl_add_u64 v[34:35], s[10:11], 0, v[2:3]
	v_lshl_add_u64 v[38:39], v[34:35], 0, s[6:7]
	s_mov_b64 s[6:7], 0x1800
	v_lshl_add_u64 v[40:41], v[34:35], 0, s[6:7]
	s_mov_b64 s[6:7], 0x1c00
	v_lshl_add_u64 v[42:43], v[34:35], 0, s[6:7]
	s_lshl_b64 s[6:7], s[0:1], 13
	v_readlane_b32 s9, v253, 3
	s_add_u32 s6, s8, s6
	s_addc_u32 s7, s9, s7
	v_readlane_b32 s12, v253, 6
	s_mov_b64 s[4:5], 0x1000
	v_lshl_add_u64 v[2:3], s[6:7], 0, v[2:3]
	s_ashr_i32 s3, s2, 31
	s_lshl_b64 s[6:7], s[0:1], 11
	s_lshl_b64 s[8:9], s[0:1], 12
	v_lshl_add_u64 v[36:37], v[34:35], 0, s[4:5]
	v_lshl_add_u64 v[44:45], v[2:3], 0, s[4:5]
	s_lshl_b64 s[4:5], s[2:3], 13
	v_lshl_or_b32 v46, v198, 2, s6
	v_mov_b32_e32 v47, s7
	s_lshl_b64 s[6:7], s[2:3], 11
	v_lshl_or_b32 v48, v198, 3, s8
	v_mov_b32_e32 v49, s9
	s_lshl_b64 s[8:9], s[2:3], 12
	v_mov_b32_e32 v54, 0x358637bd
	v_mov_b32_e32 v55, 0x3a000000
	s_mov_b32 s1, 0x800000
	s_mov_b32 s3, 0x3800000
	s_mov_b32 s10, 0xc3e00000
	v_mov_b32_e32 v56, 0x43e00000
	s_mov_b32 s11, 0x12000000
	s_mov_b32 s12, s0
	v_readlane_b32 s13, v253, 7
	v_readlane_b32 s14, v253, 8
	v_readlane_b32 s15, v253, 9
	v_readlane_b32 s16, v253, 10
	v_readlane_b32 s17, v253, 11
	v_readlane_b32 s18, v253, 12
	v_readlane_b32 s19, v253, 13
	v_readlane_b32 s20, v253, 14
	v_readlane_b32 s21, v253, 15
	v_readlane_b32 s22, v253, 16
	v_readlane_b32 s23, v253, 17
	global_load_dwordx4 v[128:131], v[34:35], off
	global_load_dwordx4 v[100:103], v[34:35], off offset:1024
	global_load_dwordx4 v[104:107], v[34:35], off offset:2048
	global_load_dwordx4 v[108:111], v[34:35], off offset:3072
	global_load_dwordx4 v[112:115], v[36:37], off
	global_load_dwordx4 v[116:119], v[38:39], off
	global_load_dwordx4 v[120:123], v[40:41], off
	global_load_dwordx4 v[124:127], v[42:43], off
.LBB0_17:
	global_load_dwordx4 v[30:33], v[44:45], off offset:-4096 nt
	global_load_dwordx4 v[26:29], v[44:45], off offset:-3072 nt
	global_load_dwordx4 v[18:21], v[44:45], off offset:-2048 nt
	global_load_dwordx4 v[10:13], v[44:45], off offset:1024 nt
	global_load_dwordx4 v[14:17], v[44:45], off nt
	global_load_dwordx4 v[22:25], v[44:45], off offset:-1024 nt
	global_load_dwordx4 v[6:9], v[44:45], off offset:2048 nt
	global_load_dwordx4 v[2:5], v[44:45], off offset:3072 nt
	s_nop 0
	s_nop 0
	v_mov_b32_e32 v85, 0
	v_mov_b32_e32 v57, 0
	v_lshl_add_u64 v[50:51], s[90:91], 0, v[48:49]
	v_add_co_u32_e32 v50, vcc, s3, v50
	v_lshl_add_u64 v[52:53], s[90:91], 0, v[46:47]
	s_nop 0
	v_addc_co_u32_e32 v51, vcc, 0, v51, vcc
	v_add_co_u32_e32 v52, vcc, s11, v52
	v_mov_b32_e32 v88, 0
	s_nop 0
	v_addc_co_u32_e32 v53, vcc, 0, v53, vcc
	s_add_i32 s12, s12, s2
	v_lshl_add_u64 v[44:45], v[44:45], 0, s[4:5]
	v_lshl_add_u64 v[46:47], v[46:47], 0, s[6:7]
	v_lshl_add_u64 v[48:49], v[48:49], 0, s[8:9]
	s_cmpk_gt_i32 s12, 0x1fff
	s_waitcnt vmcnt(7)
	v_mov_b32_e32 v64, v31
	s_waitcnt vmcnt(6)
	v_mov_b32_e32 v65, v27
	s_waitcnt vmcnt(5)
	v_pk_mul_f32 v[68:69], v[20:21], v[20:21]
	v_pk_mul_f32 v[70:71], v[18:19], v[18:19]
	s_waitcnt vmcnt(4)
	v_pk_mul_f32 v[72:73], v[12:13], v[12:13]
	v_pk_mul_f32 v[74:75], v[10:11], v[10:11]
	v_mov_b32_e32 v76, v33
	v_mov_b32_e32 v77, v29
	v_mov_b32_e32 v62, v30
	v_mov_b32_e32 v63, v26
	v_mov_b32_e32 v66, v32
	v_mov_b32_e32 v67, v28
	v_pk_mov_b32 v[86:87], v[70:71], v[68:69] op_sel:[1,0]
	v_mov_b32_e32 v71, v69
	v_pk_mov_b32 v[68:69], v[74:75], v[72:73] op_sel:[1,0]
	v_mov_b32_e32 v75, v73
	v_pk_mul_f32 v[64:65], v[64:65], v[64:65]
	v_pk_mul_f32 v[72:73], v[76:77], v[76:77]
	v_pk_fma_f32 v[62:63], v[62:63], v[62:63], v[64:65]
	v_pk_fma_f32 v[64:65], v[66:67], v[66:67], v[72:73]
	s_waitcnt vmcnt(2)
	v_mul_f32_e32 v78, v23, v23
	v_mul_f32_e32 v80, v25, v25
	v_pk_add_f32 v[66:67], v[86:87], v[70:71]
	v_pk_add_f32 v[62:63], v[62:63], v[64:65]
	v_mul_f32_e32 v89, v16, v16
	v_mul_f32_e32 v90, v17, v17
	v_mul_f32_e32 v93, v15, v15
	v_mul_f32_e32 v94, v14, v14
	v_pk_fma_f32 v[76:77], v[22:23], v[22:23], v[78:79] op_sel_hi:[1,1,0]
	v_pk_fma_f32 v[78:79], v[24:25], v[24:25], v[80:81] op_sel_hi:[1,1,0]
	v_pk_add_f32 v[66:67], v[66:67], v[66:67] op_sel:[0,1] op_sel_hi:[1,0]
	v_pk_add_f32 v[62:63], v[62:63], v[62:63] op_sel:[0,1] op_sel_hi:[1,0]
	v_mov_b32_e32 v77, v89
	v_mov_b32_e32 v79, v90
	v_mov_b32_e32 v67, v93
	v_mov_b32_e32 v63, v94
	v_pk_add_f32 v[64:65], v[76:77], v[78:79]
	v_pk_add_f32 v[62:63], v[62:63], v[66:67]
	s_waitcnt vmcnt(1)
	v_mul_f32_e32 v82, v7, v7
	v_mul_f32_e32 v84, v9, v9
	v_pk_add_f32 v[68:69], v[68:69], v[74:75]
	v_pk_add_f32 v[62:63], v[62:63], v[64:65]
	s_waitcnt vmcnt(0)
	v_mul_f32_e32 v91, v4, v4
	v_mul_f32_e32 v92, v5, v5
	v_mul_f32_e32 v95, v3, v3
	v_mul_f32_e32 v96, v2, v2
	v_pk_fma_f32 v[80:81], v[6:7], v[6:7], v[82:83] op_sel_hi:[1,1,0]
	v_pk_fma_f32 v[82:83], v[8:9], v[8:9], v[84:85] op_sel_hi:[1,1,0]
	v_pk_add_f32 v[68:69], v[68:69], v[68:69] op_sel:[0,1] op_sel_hi:[1,0]
	v_pk_add_f32 v[62:63], v[62:63], v[62:63] op_sel:[0,1] op_sel_hi:[1,0]
	v_mov_b32_e32 v81, v91
	v_mov_b32_e32 v83, v92
	v_mov_b32_e32 v69, v95
	v_mov_b32_e32 v63, v96
	v_pk_add_f32 v[70:71], v[80:81], v[82:83]
	v_pk_add_f32 v[62:63], v[62:63], v[68:69]
	s_nop 0
	v_pk_add_f32 v[62:63], v[62:63], v[70:71]
	s_nop 0
	v_add_f32_e32 v62, v62, v63
	s_nop 1
	v_add_f32_dpp v62, v62, v62 row_shr:1 row_mask:0xf bank_mask:0xf bound_ctrl:1
	s_nop 1
	v_add_f32_dpp v62, v62, v62 row_shr:2 row_mask:0xf bank_mask:0xf bound_ctrl:1
	s_nop 1
	v_add_f32_dpp v62, v62, v62 row_shr:4 row_mask:0xf bank_mask:0xf bound_ctrl:1
	s_nop 1
	v_add_f32_dpp v62, v62, v62 row_shr:8 row_mask:0xf bank_mask:0xf bound_ctrl:1
	s_nop 1
	v_mov_b32_dpp v57, v62 row_bcast:15 row_mask:0xa bank_mask:0xf
	v_add_f32_e32 v57, v62, v57
	s_nop 1
	v_mov_b32_dpp v85, v57 row_bcast:31 row_mask:0xc bank_mask:0xf
	v_add_f32_e32 v57, v57, v85
	s_nop 0
	v_readlane_b32 s13, v57, 63
	s_nop 1
	v_fma_f32 v57, s13, v55, v54
	v_mul_f32_e32 v62, 0x4b800000, v57
	v_cmp_gt_f32_e32 vcc, s1, v57
	s_nop 1
	v_cndmask_b32_e32 v57, v57, v62, vcc
	v_rsq_f32_e32 v57, v57
	s_nop 0
	v_mul_f32_e32 v62, 0x45800000, v57
	v_cndmask_b32_e32 v62, v57, v62, vcc
	v_pk_mul_f32 v[30:31], v[30:31], v[62:63] op_sel_hi:[1,0]
	v_pk_mul_f32 v[32:33], v[32:33], v[62:63] op_sel_hi:[1,0]
	s_nop 0
	v_pk_mul_f32 v[30:31], v[128:129], v[30:31]
	v_pk_mul_f32 v[32:33], v[130:131], v[32:33]
	v_cvt_pk_bf16_f32 v58, v30, v31
	v_med3_f32 v30, v30, s10, v56
	v_med3_f32 v31, v31, s10, v56
	v_cvt_pk_fp8_f32 v88, v30, v31
	v_cvt_pk_bf16_f32 v59, v32, v33
	v_med3_f32 v32, v32, s10, v56
	v_med3_f32 v33, v33, s10, v56
	v_cvt_pk_fp8_f32 v88, v32, v33 op_sel:[0,0,1]
	global_store_dwordx2 v[50:51], v[58:59], off
	v_pk_mul_f32 v[26:27], v[26:27], v[62:63] op_sel_hi:[1,0]
	v_mov_b32_e32 v57, 0
	global_store_dword v[52:53], v88, off
	s_nop 0
	s_nop 0
	v_pk_mul_f32 v[28:29], v[28:29], v[62:63] op_sel_hi:[1,0]
	v_pk_mul_f32 v[18:19], v[18:19], v[62:63] op_sel_hi:[1,0]
	v_pk_mul_f32 v[20:21], v[20:21], v[62:63] op_sel_hi:[1,0]
	v_pk_mul_f32 v[22:23], v[22:23], v[62:63] op_sel_hi:[1,0]
	v_pk_mul_f32 v[24:25], v[24:25], v[62:63] op_sel_hi:[1,0]
	v_pk_mul_f32 v[14:15], v[14:15], v[62:63] op_sel_hi:[1,0]
	v_pk_mul_f32 v[16:17], v[16:17], v[62:63] op_sel_hi:[1,0]
	v_pk_mul_f32 v[10:11], v[10:11], v[62:63] op_sel_hi:[1,0]
	v_pk_mul_f32 v[12:13], v[12:13], v[62:63] op_sel_hi:[1,0]
	v_pk_mul_f32 v[6:7], v[6:7], v[62:63] op_sel_hi:[1,0]
	v_pk_mul_f32 v[8:9], v[8:9], v[62:63] op_sel_hi:[1,0]
	v_pk_mul_f32 v[2:3], v[2:3], v[62:63] op_sel_hi:[1,0]
	v_pk_mul_f32 v[4:5], v[4:5], v[62:63] op_sel_hi:[1,0]
	s_nop 0
	v_pk_mul_f32 v[26:27], v[100:101], v[26:27]
	s_nop 0
	v_cvt_pk_bf16_f32 v30, v26, v27
	v_med3_f32 v26, v26, s10, v56
	v_med3_f32 v27, v27, s10, v56
	v_cvt_pk_fp8_f32 v57, v26, v27
	v_pk_mul_f32 v[28:29], v[102:103], v[28:29]
	s_nop 0
	v_cvt_pk_bf16_f32 v31, v28, v29
	v_med3_f32 v28, v28, s10, v56
	v_med3_f32 v29, v29, s10, v56
	v_cvt_pk_fp8_f32 v57, v28, v29 op_sel:[0,0,1]
	global_store_dwordx2 v[50:51], v[30:31], off offset:512
	v_mov_b32_e32 v30, 0
	global_store_dword v[52:53], v57, off offset:256
	s_nop 0
	s_nop 0
	s_nop 0
	v_pk_mul_f32 v[18:19], v[18:19], v[104:105]
	s_nop 0
	v_cvt_pk_bf16_f32 v26, v18, v19
	v_med3_f32 v18, v18, s10, v56
	v_med3_f32 v19, v19, s10, v56
	v_cvt_pk_fp8_f32 v30, v18, v19
	v_pk_mul_f32 v[20:21], v[20:21], v[106:107]
	s_nop 0
	v_cvt_pk_bf16_f32 v27, v20, v21
	v_med3_f32 v20, v20, s10, v56
	v_med3_f32 v21, v21, s10, v56
	v_cvt_pk_fp8_f32 v30, v20, v21 op_sel:[0,0,1]
	global_store_dwordx2 v[50:51], v[26:27], off offset:1024
	v_mov_b32_e32 v26, 0
	global_store_dword v[52:53], v30, off offset:512
	s_nop 0
	s_nop 0
	s_nop 0
	v_pk_mul_f32 v[18:19], v[22:23], v[108:109]
	s_nop 0
	v_cvt_pk_bf16_f32 v22, v18, v19
	v_med3_f32 v18, v18, s10, v56
	v_med3_f32 v19, v19, s10, v56
	v_cvt_pk_fp8_f32 v26, v18, v19
	v_pk_mul_f32 v[20:21], v[24:25], v[110:111]
	s_nop 0
	v_cvt_pk_bf16_f32 v23, v20, v21
	v_med3_f32 v20, v20, s10, v56
	v_med3_f32 v21, v21, s10, v56
	v_cvt_pk_fp8_f32 v26, v20, v21 op_sel:[0,0,1]
	global_store_dwordx2 v[50:51], v[22:23], off offset:1536
	v_mov_b32_e32 v22, 0
	global_store_dword v[52:53], v26, off offset:768
	s_nop 0
	s_nop 0
	s_nop 0
	v_pk_mul_f32 v[14:15], v[14:15], v[112:113]
	s_nop 0
	v_cvt_pk_bf16_f32 v18, v14, v15
	v_med3_f32 v14, v14, s10, v56
	v_med3_f32 v15, v15, s10, v56
	v_cvt_pk_fp8_f32 v22, v14, v15
	v_pk_mul_f32 v[16:17], v[16:17], v[114:115]
	s_nop 0
	v_cvt_pk_bf16_f32 v19, v16, v17
	v_med3_f32 v16, v16, s10, v56
	v_med3_f32 v17, v17, s10, v56
	v_cvt_pk_fp8_f32 v22, v16, v17 op_sel:[0,0,1]
	global_store_dwordx2 v[50:51], v[18:19], off offset:2048
	v_mov_b32_e32 v18, 0
	global_store_dword v[52:53], v22, off offset:1024
	s_nop 0
	s_nop 0
	s_nop 0
	v_pk_mul_f32 v[10:11], v[10:11], v[116:117]
	s_nop 0
	v_cvt_pk_bf16_f32 v14, v10, v11
	v_med3_f32 v10, v10, s10, v56
	v_med3_f32 v11, v11, s10, v56
	v_cvt_pk_fp8_f32 v18, v10, v11
	v_pk_mul_f32 v[12:13], v[12:13], v[118:119]
	s_nop 0
	v_cvt_pk_bf16_f32 v15, v12, v13
	v_med3_f32 v12, v12, s10, v56
	v_med3_f32 v13, v13, s10, v56
	v_cvt_pk_fp8_f32 v18, v12, v13 op_sel:[0,0,1]
	global_store_dwordx2 v[50:51], v[14:15], off offset:2560
	v_mov_b32_e32 v14, 0
	global_store_dword v[52:53], v18, off offset:1280
	s_nop 0
	s_nop 0
	s_nop 0
	v_pk_mul_f32 v[6:7], v[6:7], v[120:121]
	s_nop 0
	v_cvt_pk_bf16_f32 v10, v6, v7
	v_med3_f32 v6, v6, s10, v56
	v_med3_f32 v7, v7, s10, v56
	v_cvt_pk_fp8_f32 v14, v6, v7
	v_pk_mul_f32 v[8:9], v[8:9], v[122:123]
	s_nop 0
	v_med3_f32 v6, v8, s10, v56
	v_med3_f32 v7, v9, s10, v56
	v_cvt_pk_fp8_f32 v14, v6, v7 op_sel:[0,0,1]
	v_cvt_pk_bf16_f32 v11, v8, v9
	global_store_dwordx2 v[50:51], v[10:11], off offset:3072
	global_store_dword v[52:53], v14, off offset:1536
	s_nop 0
	s_nop 0
	v_mov_b32_e32 v10, 0
	s_nop 0
	v_pk_mul_f32 v[2:3], v[2:3], v[124:125]
	s_nop 0
	v_med3_f32 v6, v2, s10, v56
	v_med3_f32 v7, v3, s10, v56
	v_cvt_pk_fp8_f32 v10, v6, v7
	v_pk_mul_f32 v[4:5], v[4:5], v[126:127]
	v_cvt_pk_bf16_f32 v2, v2, v3
	v_med3_f32 v6, v4, s10, v56
	v_med3_f32 v7, v5, s10, v56
	v_cvt_pk_fp8_f32 v10, v6, v7 op_sel:[0,0,1]
	v_cvt_pk_bf16_f32 v3, v4, v5
	global_store_dwordx2 v[50:51], v[2:3], off offset:3584
	global_store_dword v[52:53], v10, off offset:1792
	s_cbranch_scc0 .LBB0_17
